# attention-A side-work finish: per-lane constants from a per-wave LDS table (written once per unit into the free third ring slots), saddr-form stores with a scalar base stepped by SALU, scalar-operand
# speedup vs baseline: 1.0064x; 1.0064x over previous
.Lpro_noconv:
	s_cmp_lg_u64 s[12:13], 0
	s_cselect_b64 s[54:55], -1, 0
	s_cmp_lt_u32 s0, 2
	s_mov_b32 s0, 0x3f400000
	s_cselect_b64 s[52:53], -1, 0
	s_mov_b32 s8, s9
	v_mfma_scale_f32_32x32x64_f8f6f4 v[16:31], v[12:17], v[182:187], 0, v217, v216 op_sel_hi:[0,0,0] cbsz:2 blgp:2
	s_nop 4
	v_max_f32_e32 v52, v33, v33
	v_max_f32_e32 v53, v32, v32
	v_max_f32_e32 v52, v53, v52
	v_max3_f32 v52, v52, v34, v35
	v_max3_f32 v52, v52, v36, v37
	v_max3_f32 v52, v52, v38, v39
	v_max3_f32 v52, v52, v40, v41
	v_mfma_scale_f32_32x32x64_f8f6f4 v[16:31], v[58:63], v[176:181], v[16:31], v217, v216 op_sel_hi:[0,0,0] cbsz:2 blgp:2
	v_max3_f32 v52, v52, v42, v43
	v_max3_f32 v52, v52, v44, v45
	v_max3_f32 v52, v52, v46, v47
	s_mov_b32 s10, s9
	s_mov_b32 s11, s9
	s_mov_b32 s12, s9
	s_mov_b32 s13, s9
	s_nop 4
	v_max3_f32 v52, v52, v16, v17
	v_max3_f32 v52, v52, v18, v19
	v_max3_f32 v52, v52, v20, v21
	v_max3_f32 v52, v52, v22, v23
	v_max3_f32 v52, v52, v24, v25
	v_max3_f32 v52, v52, v26, v27
	v_max3_f32 v52, v52, v28, v29
	v_max3_f32 v52, v52, v30, v31
	v_mov_b32_e32 v53, v52
	s_nop 1
	v_permlane32_swap_b32_e32 v52, v53
	v_max_f32_e32 v53, v53, v53
	v_max_f32_e32 v52, v52, v52
	v_max_f32_e32 v52, v52, v53
	v_add_f32_e32 v53, 0x7149f2ca, v52
	v_cmp_ge_f32_e32 vcc, s0, v53
	v_max_f32_e32 v52, 0xf149f2ca, v52
	s_cmp_lg_u64 vcc, exec
	v_add_f32_e32 v52, 2.0, v52
	s_cselect_b64 vcc, -1, 0
	v_cndmask_b32_e32 v52, v219, v52, vcc
	v_add_f32_e32 v53, -4.0, v52
	s_lshl_b32 s0, s46, 2
	v_sub_f32_e32 v32, v32, v53
	v_sub_f32_e32 v33, v33, v53
	v_sub_f32_e32 v34, v34, v53
	v_sub_f32_e32 v35, v35, v53
	v_sub_f32_e32 v36, v36, v53
	v_sub_f32_e32 v37, v37, v53
	v_sub_f32_e32 v38, v38, v53
	v_sub_f32_e32 v39, v39, v53
	v_sub_f32_e32 v40, v40, v53
	v_sub_f32_e32 v41, v41, v53
	v_sub_f32_e32 v42, v42, v53
	v_sub_f32_e32 v43, v43, v53
	v_sub_f32_e32 v44, v44, v53
	v_sub_f32_e32 v45, v45, v53
	v_sub_f32_e32 v46, v46, v53
	v_sub_f32_e32 v47, v47, v53
	s_add_i32 s0, s0, 0
	s_mov_b32 s14, s9
	s_mov_b32 s15, s9
	s_mov_b32 s16, s9
	s_mov_b32 s17, s9
	s_mov_b32 s18, s9
	s_mov_b32 s19, s9
	s_mov_b32 s20, s9
	s_mov_b32 s21, s9
	s_mov_b32 s22, s9
	s_mov_b32 s23, s9
	v_mov_b64_e32 v[0:1], s[8:9]
	v_exp_f32_e32 v144, v32
	v_exp_f32_e32 v145, v33
	v_exp_f32_e32 v146, v34
	v_exp_f32_e32 v147, v35
	v_exp_f32_e32 v148, v36
	v_exp_f32_e32 v149, v37
	v_exp_f32_e32 v150, v38
	v_exp_f32_e32 v151, v39
	v_exp_f32_e32 v152, v40
	v_exp_f32_e32 v153, v41
	v_exp_f32_e32 v154, v42
	v_exp_f32_e32 v155, v43
	v_exp_f32_e32 v156, v44
	v_exp_f32_e32 v157, v45
	v_exp_f32_e32 v158, v46
	v_exp_f32_e32 v159, v47
	s_add_i32 s0, s0, 0x1c800
	v_mov_b64_e32 v[2:3], s[10:11]
	v_mov_b64_e32 v[4:5], s[12:13]
	v_mov_b64_e32 v[6:7], s[14:15]
	v_mov_b64_e32 v[8:9], s[16:17]
	v_mov_b64_e32 v[10:11], s[18:19]
	v_mov_b64_e32 v[12:13], s[20:21]
	v_mov_b64_e32 v[14:15], s[22:23]
	v_sub_f32_e32 v128, v16, v53
	s_and_b64 s[10:11], s[52:53], exec
	v_lshlrev_b32_e32 v16, 7, v48
	v_sub_f32_e32 v80, 4.0, v52
	v_sub_f32_e32 v143, v31, v53
	v_sub_f32_e32 v142, v30, v53
	v_sub_f32_e32 v141, v29, v53
	v_sub_f32_e32 v140, v28, v53
	v_sub_f32_e32 v139, v27, v53
	v_sub_f32_e32 v138, v26, v53
	v_sub_f32_e32 v137, v25, v53
	v_sub_f32_e32 v136, v24, v53
	v_sub_f32_e32 v135, v23, v53
	v_sub_f32_e32 v134, v22, v53
	v_sub_f32_e32 v133, v21, v53
	v_sub_f32_e32 v132, v20, v53
	v_sub_f32_e32 v131, v19, v53
	v_sub_f32_e32 v130, v18, v53
	v_sub_f32_e32 v129, v17, v53
	s_cselect_b32 s14, 23, 22
	v_add3_u32 v164, s85, v16, v51
	s_add_u32 s10, s78, s4
	v_add_u32_e32 v174, v49, v50
	v_mov_b64_e32 v[62:63], v[14:15]
	v_mov_b64_e32 v[46:47], v[14:15]
	v_mov_b64_e32 v[30:31], v[14:15]
	v_mov_b64_e32 v[78:79], v[14:15]
	s_mov_b32 s1, 2
	s_mov_b32 s57, 1
	s_mov_b32 s27, -2
	v_mov_b32_e32 v81, v80
	v_mov_b32_e32 v82, v80
	v_mov_b32_e32 v83, v80
	v_mov_b32_e32 v84, v80
	v_mov_b32_e32 v85, v80
	v_mov_b32_e32 v86, v80
	v_mov_b32_e32 v87, v80
	v_mov_b32_e32 v88, v80
	v_mov_b32_e32 v89, v80
	v_mov_b32_e32 v90, v80
	v_mov_b32_e32 v91, v80
	v_mov_b32_e32 v92, v80
	v_mov_b32_e32 v93, v80
	v_mov_b32_e32 v94, v80
	v_mov_b32_e32 v95, v80
	s_mov_b32 s15, 0
	v_mov_b32_e32 v165, v167
	s_addc_u32 s11, s79, s5
	v_mov_b32_e32 v175, v167
	v_mov_b64_e32 v[60:61], v[12:13]
	v_mov_b64_e32 v[58:59], v[10:11]
	v_mov_b64_e32 v[56:57], v[8:9]
	v_mov_b64_e32 v[54:55], v[6:7]
	v_mov_b64_e32 v[52:53], v[4:5]
	v_mov_b64_e32 v[50:51], v[2:3]
	v_mov_b64_e32 v[48:49], v[0:1]
	v_mov_b64_e32 v[44:45], v[12:13]
	v_mov_b64_e32 v[42:43], v[10:11]
	v_mov_b64_e32 v[40:41], v[8:9]
	v_mov_b64_e32 v[38:39], v[6:7]
	v_mov_b64_e32 v[36:37], v[4:5]
	v_mov_b64_e32 v[34:35], v[2:3]
	v_mov_b64_e32 v[32:33], v[0:1]
	v_mov_b64_e32 v[28:29], v[12:13]
	v_mov_b64_e32 v[26:27], v[10:11]
	v_mov_b64_e32 v[24:25], v[8:9]
	v_mov_b64_e32 v[22:23], v[6:7]
	v_mov_b64_e32 v[20:21], v[4:5]
	v_mov_b64_e32 v[18:19], v[2:3]
	v_mov_b64_e32 v[16:17], v[0:1]
	s_mov_b32 s16, 2
	v_mov_b64_e32 v[76:77], v[12:13]
	v_mov_b64_e32 v[74:75], v[10:11]
	v_mov_b64_e32 v[72:73], v[8:9]
	v_mov_b64_e32 v[70:71], v[6:7]
	v_mov_b64_e32 v[68:69], v[4:5]
	v_mov_b64_e32 v[66:67], v[2:3]
	v_mov_b64_e32 v[64:65], v[0:1]
	v_mbcnt_lo_u32_b32 v200, -1, 0
	v_mbcnt_hi_u32_b32 v200, -1, v200
	v_lshrrev_b32_e32 v201, 3, v200
	v_mul_lo_u32 v201, v201, s56
	v_lshlrev_b32_e32 v200, 4, v200
	v_and_b32_e32 v200, 0x70, v200
	v_lshl_or_b32 v214, v201, 2, v200
	v_mov_b32_e32 v215, v214
	s_mov_b64 s[98:99], s[58:59]
	s_add_i32 s100, s66, 0xc800
	s_lshl_b32 s101, s56, 5
	s_movk_i32 s17, 0x70
	ds_read_b128 v[228:231], v223 offset:8192
	ds_read_b64 v[232:233], v224 offset:8192
	ds_read_b128 v[234:237], v223 offset:12288
	ds_read_b64 v[238:239], v224 offset:12288
	ds_read_b128 v[240:243], v221 offset:8192
	ds_read_b64 v[244:245], v222 offset:8192
	ds_read_b128 v[246:249], v221 offset:12288
	ds_read_b64 v[250:251], v222 offset:12288
	v_mbcnt_lo_u32_b32 v200, -1, 0
	v_mbcnt_hi_u32_b32 v200, -1, v200
	v_and_b32_e32 v201, 7, v200
	v_ashrrev_i32_e32 v202, 3, v200
	v_lshlrev_b32_e32 v203, 2, v200
	v_lshl_add_u32 v204, v201, 10, s66
	v_lshlrev_b32_e32 v205, 2, v202
	v_and_b32_e32 v205, 12, v205
	v_add_u32_e32 v204, 0xc800, v204
	v_add_u32_e32 v204, v204, v205
	v_add_u32_e32 v206, v202, v203
	v_add_u32_e32 v207, 8, v206
	v_add_u32_e32 v208, 16, v206
	v_add_u32_e32 v209, 24, v206
	v_and_b32_e32 v206, 28, v206
	v_and_b32_e32 v207, 28, v207
	v_and_b32_e32 v208, 28, v208
	v_and_b32_e32 v209, 28, v209
	v_lshl_add_u32 v206, v206, 2, v204
	v_lshl_add_u32 v207, v207, 2, v204
	v_lshl_add_u32 v208, v208, 2, v204
	v_lshl_add_u32 v209, v209, 2, v204
	v_mul_u32_u24_e32 v210, s48, v202
	v_lshl_add_u32 v210, v201, 3, v210
	v_lshl_add_u32 v211, v201, 5, s0
	v_lshl_add_u32 v205, v200, 4, s89
	ds_write_b128 v205, v[206:209] offset:16384
	ds_write_b64 v205, v[210:211] offset:40960

.LBB0_432:
	s_waitcnt vmcnt(2)
	v_mbcnt_lo_u32_b32 v138, -1, 0
	v_mbcnt_hi_u32_b32 v138, -1, v138
	s_lshr_b32 s8, s1, 3
	s_add_i32 s12, s8, -1
	s_ashr_i32 s13, s12, 31
	s_lshl_b64 s[12:13], s[12:13], s14
	v_lshl_add_u32 v138, v138, 4, s89
	s_add_u32 s12, s50, s12
	s_addc_u32 s13, s51, s13
	ds_read_b128 v[150:153], v138 offset:16384
	ds_read_b64 v[146:147], v138 offset:40960
	s_mul_hi_u32 s19, s44, s48
	s_mul_i32 s18, s44, s48
	s_add_u32 s12, s12, s18
	s_addc_u32 s13, s13, s19
	s_add_u32 s12, s12, s46
	s_addc_u32 s13, s13, s47
	s_lshl_b32 s18, s48, 3
	s_andn2_b64 vcc, exec, s[54:55]
	s_waitcnt lgkmcnt(0)
	s_cbranch_vccnz .Lfin_nog
	ds_read_b128 v[128:131], v147
	ds_read_b128 v[140:143], v147 offset:16
.Lfin_nog:
	ds_read2_b32 v[188:189], v150 offset0:0 offset1:32
	ds_read2_b32 v[190:191], v150 offset0:64 offset1:96
	ds_read2_b32 v[192:193], v150 offset0:128 offset1:160
	ds_read2_b32 v[194:195], v150 offset0:192 offset1:224
	ds_read2_b32 v[196:197], v151 offset0:0 offset1:32
	ds_read2_b32 v[198:199], v151 offset0:64 offset1:96
	ds_read2_b32 v[200:201], v151 offset0:128 offset1:160
	ds_read2_b32 v[202:203], v151 offset0:192 offset1:224
	s_waitcnt lgkmcnt(7)
	ds_read2_b32 v[204:205], v152 offset0:0 offset1:32
	ds_read2_b32 v[206:207], v152 offset0:64 offset1:96
	ds_read2_b32 v[208:209], v152 offset0:128 offset1:160
	ds_read2_b32 v[210:211], v152 offset0:192 offset1:224
	ds_read2_b32 v[154:155], v153 offset0:0 offset1:32
	ds_read2_b32 v[156:157], v153 offset0:64 offset1:96
	ds_read2_b32 v[158:159], v153 offset0:128 offset1:160
	ds_read2_b32 v[212:213], v153 offset0:192 offset1:224
	s_cbranch_vccnz .Lfin_const
	s_waitcnt lgkmcnt(0)
	v_pk_mul_f32 v[132:133], v[130:131], s[24:25] op_sel_hi:[1,0]
	v_pk_mul_f32 v[134:135], v[128:129], s[24:25] op_sel_hi:[1,0]
	v_pk_mul_f32 v[128:129], v[142:143], s[24:25] op_sel_hi:[1,0]
	v_pk_mul_f32 v[130:131], v[140:141], s[24:25] op_sel_hi:[1,0]
	v_pk_mul_f32 v[188:189], v[188:189], v[134:135]
	v_pk_mul_f32 v[190:191], v[190:191], v[132:133]
	v_pk_mul_f32 v[192:193], v[192:193], v[130:131]
	v_pk_mul_f32 v[194:195], v[194:195], v[128:129]
	v_cvt_pk_fp8_f32 v140, v188, v189
	v_cvt_pk_fp8_f32 v141, v192, v193
	v_cvt_pk_fp8_f32 v140, v190, v191 op_sel:[0,0,1]
	v_cvt_pk_fp8_f32 v141, v194, v195 op_sel:[0,0,1]
	s_nop 1
	global_store_dwordx2 v146, v[140:141], s[12:13] nt
	s_add_u32 s12, s12, s18
	s_addc_u32 s13, s13, 0
	v_pk_mul_f32 v[196:197], v[196:197], v[134:135]
	v_pk_mul_f32 v[198:199], v[198:199], v[132:133]
	v_pk_mul_f32 v[200:201], v[200:201], v[130:131]
	v_pk_mul_f32 v[202:203], v[202:203], v[128:129]
	v_cvt_pk_fp8_f32 v142, v196, v197
	v_cvt_pk_fp8_f32 v143, v200, v201
	v_cvt_pk_fp8_f32 v142, v198, v199 op_sel:[0,0,1]
	v_cvt_pk_fp8_f32 v143, v202, v203 op_sel:[0,0,1]
	s_nop 1
	global_store_dwordx2 v146, v[142:143], s[12:13] nt
	s_add_u32 s12, s12, s18
	s_addc_u32 s13, s13, 0
	v_pk_mul_f32 v[204:205], v[204:205], v[134:135]
	v_pk_mul_f32 v[206:207], v[206:207], v[132:133]
	v_pk_mul_f32 v[208:209], v[208:209], v[130:131]
	v_pk_mul_f32 v[210:211], v[210:211], v[128:129]
	v_cvt_pk_fp8_f32 v140, v204, v205
	v_cvt_pk_fp8_f32 v141, v208, v209
	v_cvt_pk_fp8_f32 v140, v206, v207 op_sel:[0,0,1]
	v_cvt_pk_fp8_f32 v141, v210, v211 op_sel:[0,0,1]
	s_nop 1
	global_store_dwordx2 v146, v[140:141], s[12:13] nt
	s_add_u32 s12, s12, s18
	s_addc_u32 s13, s13, 0
	v_pk_mul_f32 v[154:155], v[154:155], v[134:135]
	v_pk_mul_f32 v[156:157], v[156:157], v[132:133]
	v_pk_mul_f32 v[158:159], v[158:159], v[130:131]
	v_pk_mul_f32 v[212:213], v[212:213], v[128:129]
	v_cvt_pk_fp8_f32 v142, v154, v155
	v_cvt_pk_fp8_f32 v143, v158, v159
	v_cvt_pk_fp8_f32 v142, v156, v157 op_sel:[0,0,1]
	v_cvt_pk_fp8_f32 v143, v212, v213 op_sel:[0,0,1]
	s_nop 1
	global_store_dwordx2 v146, v[142:143], s[12:13] nt
	s_branch .Lfin_done
.Lfin_const:
	s_waitcnt lgkmcnt(0)
	v_pk_mul_f32 v[188:189], v[188:189], s[24:25] op_sel_hi:[1,0]
	v_pk_mul_f32 v[190:191], v[190:191], s[24:25] op_sel_hi:[1,0]
	v_pk_mul_f32 v[192:193], v[192:193], s[24:25] op_sel_hi:[1,0]
	v_pk_mul_f32 v[194:195], v[194:195], s[24:25] op_sel_hi:[1,0]
	v_cvt_pk_fp8_f32 v140, v188, v189
	v_cvt_pk_fp8_f32 v141, v192, v193
	v_cvt_pk_fp8_f32 v140, v190, v191 op_sel:[0,0,1]
	v_cvt_pk_fp8_f32 v141, v194, v195 op_sel:[0,0,1]
	s_nop 1
	global_store_dwordx2 v146, v[140:141], s[12:13] nt
	s_add_u32 s12, s12, s18
	s_addc_u32 s13, s13, 0
	v_pk_mul_f32 v[196:197], v[196:197], s[24:25] op_sel_hi:[1,0]
	v_pk_mul_f32 v[198:199], v[198:199], s[24:25] op_sel_hi:[1,0]
	v_pk_mul_f32 v[200:201], v[200:201], s[24:25] op_sel_hi:[1,0]
	v_pk_mul_f32 v[202:203], v[202:203], s[24:25] op_sel_hi:[1,0]
	v_cvt_pk_fp8_f32 v142, v196, v197
	v_cvt_pk_fp8_f32 v143, v200, v201
	v_cvt_pk_fp8_f32 v142, v198, v199 op_sel:[0,0,1]
	v_cvt_pk_fp8_f32 v143, v202, v203 op_sel:[0,0,1]
	s_nop 1
	global_store_dwordx2 v146, v[142:143], s[12:13] nt
	s_add_u32 s12, s12, s18
	s_addc_u32 s13, s13, 0
	v_pk_mul_f32 v[204:205], v[204:205], s[24:25] op_sel_hi:[1,0]
	v_pk_mul_f32 v[206:207], v[206:207], s[24:25] op_sel_hi:[1,0]
	v_pk_mul_f32 v[208:209], v[208:209], s[24:25] op_sel_hi:[1,0]
	v_pk_mul_f32 v[210:211], v[210:211], s[24:25] op_sel_hi:[1,0]
	v_cvt_pk_fp8_f32 v140, v204, v205
	v_cvt_pk_fp8_f32 v141, v208, v209
	v_cvt_pk_fp8_f32 v140, v206, v207 op_sel:[0,0,1]
	v_cvt_pk_fp8_f32 v141, v210, v211 op_sel:[0,0,1]
	s_nop 1
	global_store_dwordx2 v146, v[140:141], s[12:13] nt
	s_add_u32 s12, s12, s18
	s_addc_u32 s13, s13, 0
	v_pk_mul_f32 v[154:155], v[154:155], s[24:25] op_sel_hi:[1,0]
	v_pk_mul_f32 v[156:157], v[156:157], s[24:25] op_sel_hi:[1,0]
	v_pk_mul_f32 v[158:159], v[158:159], s[24:25] op_sel_hi:[1,0]
	v_pk_mul_f32 v[212:213], v[212:213], s[24:25] op_sel_hi:[1,0]
	v_cvt_pk_fp8_f32 v142, v154, v155
	v_cvt_pk_fp8_f32 v143, v158, v159
	v_cvt_pk_fp8_f32 v142, v156, v157 op_sel:[0,0,1]
	v_cvt_pk_fp8_f32 v143, v212, v213 op_sel:[0,0,1]
	s_nop 1
	global_store_dwordx2 v146, v[142:143], s[12:13] nt
.Lfin_done:
	s_lshl_b64 s[98:99], s[8:9], 24
	s_add_u32 s98, s58, s98
	s_addc_u32 s99, s59, s99
	s_add_i32 s100, s66, 0xc800
	v_mov_b32_e32 v215, v214
	s_mov_b32 m0, s100
	s_nop 0
	global_load_lds_dwordx4 v215, s[98:99] nt
	s_branch .LBB0_437
